# attention phase: one static s_setprio 1 for waves 4-7 (younger-half priority raise), reset at phase exit; five redundant scalar/vector instructions removed from the inner loop
# speedup vs baseline: 1.0106x; 1.0013x over previous
.LBB0_1190:
	v_readlane_b32 s10, v254, 0
	s_cmp_le_i32 s10, s0
	s_cselect_b64 s[0:1], -1, 0
	s_and_b64 s[18:19], s[0:1], s[26:27]
	s_andn2_b64 vcc, exec, s[18:19]
	v_readlane_b32 s11, v254, 1
	s_cbranch_vccnz .LBB0_1368
	s_mov_b32 s100, m0
	v_readlane_b32 s12, v254, 2
	v_readlane_b32 s14, v254, 4
	v_readlane_b32 s15, v254, 5
	s_waitcnt lgkmcnt(0)
	s_mov_b64 s[36:37], s[14:15]
	s_mov_b32 s0, s2
	v_readlane_b32 s13, v254, 3
	s_mov_b64 s[0:1], s[12:13]
	v_mov_b32_e32 v178, v0
	v_readfirstlane_b32 s101, v0
	s_nop 3
	s_and_b32 s101, s101, 0x3ff
	s_lshr_b32 s101, s101, 6
	s_cmp_ge_u32 s101, 4
	s_cbranch_scc0 .Lattn_prio_done
	s_setprio 1
.Lattn_prio_done:
	s_mov_b32 s28, 13
	v_and_b32_e32 v169, 63, v178
	v_cmp_gt_u32_e32 vcc, 16, v169
	v_mov_b32_e32 v185, 0x63
	s_and_saveexec_b64 s[26:27], vcc
	s_cbranch_execz .LBB0_1253
	v_readlane_b32 s0, v254, 63
	v_readlane_b32 s1, v255, 0
	s_ashr_i32 s29, s28, 31
	s_lshl_b32 s66, s0, 4
	s_lshl_b64 s[0:1], s[28:29], 3
	s_add_u32 s0, s94, s0
	s_addc_u32 s1, s95, s1
	s_load_dwordx2 s[0:1], s[0:1], 0x0
	s_lshl_b64 s[10:11], s[66:67], 2
	v_lshlrev_b32_e32 v166, 2, v169
	s_waitcnt lgkmcnt(0)
	s_add_u32 s28, s0, s10
	s_addc_u32 s29, s1, s11
	s_waitcnt vmcnt(0)
	v_lshl_add_u64 v[2:3], s[28:29], 0, v[166:167]
	v_mov_b64_e32 v[4:5], s[28:29]
	flat_load_dword v2, v[2:3]
	s_nop 0
	flat_load_dword v5, v[4:5]
	v_mov_b32_e32 v3, 1
	v_mov_b32_e32 v4, 1
	s_waitcnt vmcnt(0) lgkmcnt(0)
	v_cmp_ngt_f32_e32 vcc, v5, v2
	s_and_saveexec_b64 s[30:31], vcc
	s_cbranch_execz .LBB0_1196
	v_cmp_eq_f32_e32 vcc, v5, v2
	v_mov_b32_e32 v4, 0
	s_and_saveexec_b64 s[34:35], vcc
	v_cmp_ne_u32_e32 vcc, 0, v169
	s_nop 1
	v_cndmask_b32_e64 v4, 0, 1, vcc
	s_or_b64 exec, exec, s[34:35]

.LBB0_1319:
	s_add_i32 s45, s44, -2
	s_mul_hi_i32 s50, s45, 0x55555556
	s_mul_i32 s50, s50, 3
	s_sub_i32 s45, s45, s50
	v_lshl_add_u32 v162, s45, 13, v240
	ds_read_b64_tr_b16 v[142:143], v162 offset:40960
	ds_read_b64_tr_b16 v[144:145], v162 offset:41472
	s_add_i32 s45, s44, -1
	v_mfma_f32_32x32x16_bf16 v[82:97], v[138:141], v[98:101], 0
	v_add_f32_e32 v66, v50, v51
	v_add_f32_e32 v67, v52, v53
	v_add_f32_e32 v66, v66, v67
	v_cvt_pk_bf16_f32 v138, v50, v51
	v_cvt_pk_bf16_f32 v139, v52, v53
	ds_read_b64_tr_b16 v[146:147], v162 offset:45056
	ds_read_b64_tr_b16 v[148:149], v162 offset:45568
	v_add_f32_e32 v50, v54, v55
	v_add_f32_e32 v51, v56, v57
	v_add_f32_e32 v50, v50, v51
	v_add_f32_e32 v50, v50, v66
	v_mfma_f32_32x32x16_bf16 v[66:81], v[130:133], v[98:101], 0
	v_cvt_pk_bf16_f32 v140, v54, v55
	v_cvt_pk_bf16_f32 v141, v56, v57
	s_and_b32 s50, s45, 3
	s_mulk_i32 s50, 0x2800
	v_add_u32_e32 v150, s50, v238
	ds_read_b128 v[130:133], v150 offset:6144
	ds_read_b128 v[158:161], v150 offset:6656
	ds_read_b64_tr_b16 v[54:55], v162 offset:41984
	ds_read_b64_tr_b16 v[56:57], v162 offset:42496
	v_mfma_f32_32x32x16_bf16 v[82:97], v[134:137], v[102:105], v[82:97]
	v_add_f32_e32 v51, v58, v59
	v_add_f32_e32 v52, v60, v61
	v_add_f32_e32 v51, v51, v52
	v_add_f32_e32 v52, v51, v50
	v_cvt_pk_bf16_f32 v50, v58, v59
	v_cvt_pk_bf16_f32 v51, v60, v61
	ds_read_b64_tr_b16 v[58:59], v162 offset:46080
	ds_read_b64_tr_b16 v[60:61], v162 offset:46592
	v_mfma_f32_32x32x16_bf16 v[66:81], v[126:129], v[102:105], v[66:81]
	v_add_f32_e32 v53, v62, v63
	v_add_f32_e32 v126, v64, v65
	v_add_f32_e32 v53, v53, v126
	v_add_f32_e32 v151, v53, v52
	v_cvt_pk_bf16_f32 v52, v62, v63
	v_cvt_pk_bf16_f32 v53, v64, v65
	ds_read_b128 v[126:129], v150 offset:8192
	ds_read_b128 v[134:137], v150 offset:8704
	ds_read_b64_tr_b16 v[62:63], v162 offset:43008
	ds_read_b64_tr_b16 v[64:65], v162 offset:43520
	v_mfma_f32_32x32x16_bf16 v[82:97], v[122:125], v[106:109], v[82:97]
	v_add_f32_e32 v122, v34, v35
	v_add_f32_e32 v123, v36, v37
	v_add_f32_e32 v122, v122, v123
	v_add_f32_e32 v122, v122, v151
	v_cvt_pk_bf16_f32 v34, v34, v35
	v_cvt_pk_bf16_f32 v35, v36, v37
	ds_read_b64_tr_b16 v[150:151], v162 offset:47104
	ds_read_b64_tr_b16 v[152:153], v162 offset:47616
	v_mfma_f32_32x32x16_bf16 v[66:81], v[118:121], v[106:109], v[66:81]
	v_add_f32_e32 v36, v38, v39
	v_add_f32_e32 v37, v40, v41
	v_add_f32_e32 v36, v36, v37
	v_add_f32_e32 v118, v36, v122
	v_cvt_pk_bf16_f32 v36, v38, v39
	v_cvt_pk_bf16_f32 v37, v40, v41
	ds_read_b64_tr_b16 v[154:155], v162 offset:44032
	ds_read_b64_tr_b16 v[156:157], v162 offset:44544
	s_waitcnt lgkmcnt(13)
	v_mfma_f32_32x32x16_bf16 v[82:97], v[130:133], v[110:113], v[82:97]
	v_add_f32_e32 v38, v42, v43
	v_add_f32_e32 v39, v44, v45
	v_add_f32_e32 v38, v38, v39
	v_add_f32_e32 v40, v38, v118
	v_cvt_pk_bf16_f32 v38, v42, v43
	v_cvt_pk_bf16_f32 v39, v44, v45
	ds_read_b64_tr_b16 v[42:43], v162 offset:48128
	ds_read_b64_tr_b16 v[44:45], v162 offset:48640
	s_waitcnt lgkmcnt(14)
	v_mfma_f32_32x32x16_bf16 v[66:81], v[158:161], v[110:113], v[66:81]
	v_add_f32_e32 v41, v46, v47
	v_add_f32_e32 v118, v48, v49
	v_add_f32_e32 v41, v41, v118
	v_add_f32_e32 v166, v41, v40
	v_cvt_pk_bf16_f32 v40, v46, v47
	v_cvt_pk_bf16_f32 v41, v48, v49
	s_waitcnt lgkmcnt(9)
	v_mfma_f32_32x32x16_bf16 v[82:97], v[126:129], v[114:117], v[82:97]
	s_waitcnt lgkmcnt(8)
	v_mfma_f32_32x32x16_bf16 v[66:81], v[134:137], v[114:117], v[66:81]
	s_add_i32 s61, s44, 2
	s_cmp_lt_i32 s61, s71
	s_cselect_b64 s[52:53], -1, 0
	s_cmp_ge_i32 s61, s71
	s_cselect_b64 s[50:51], -1, 0
	s_cbranch_scc1 .LBB0_1322
	s_and_b32 s54, s61, 3
	s_mulk_i32 s54, 0x2800
	s_add_i32 s55, s54, s66
	s_mov_b32 m0, s55
	s_nop 0
	global_load_lds_dwordx4 v[222:223], off
	s_and_b64 vcc, exec, s[42:43]
	s_cbranch_vccnz .LBB0_1322
	s_add_i32 s54, s54, s70
	s_mov_b32 m0, s54
	s_nop 0
	global_load_lds_dwordx4 v[220:221], off

.LBB0_1331:
	s_mul_hi_i32 s52, s45, 0x55555556
	s_mul_i32 s52, s52, 3
	s_sub_i32 s45, s45, s52
	v_lshl_add_u32 v199, s45, 13, v240
	ds_read_b64_tr_b16 v[162:163], v199 offset:40960
	ds_read_b64_tr_b16 v[164:165], v199 offset:41472
	s_waitcnt lgkmcnt(7)
	v_mfma_f32_32x32x16_bf16 v[50:65], v[138:141], v[98:101], 0
	v_add_f32_e32 v34, v82, v83
	v_add_f32_e32 v35, v84, v85
	v_add_f32_e32 v34, v34, v35
	v_cvt_pk_bf16_f32 v154, v82, v83
	v_cvt_pk_bf16_f32 v155, v84, v85
	ds_read_b64_tr_b16 v[158:159], v199 offset:45056
	ds_read_b64_tr_b16 v[160:161], v199 offset:45568
	v_add_f32_e32 v35, v86, v87
	v_add_f32_e32 v36, v88, v89
	v_add_f32_e32 v35, v35, v36
	v_add_f32_e32 v82, v35, v34
	s_waitcnt lgkmcnt(8)
	v_mfma_f32_32x32x16_bf16 v[34:49], v[130:133], v[98:101], 0
	v_cvt_pk_bf16_f32 v156, v86, v87
	v_cvt_pk_bf16_f32 v157, v88, v89
	ds_read_b128 v[170:173], v197 offset:6144
	ds_read_b128 v[174:177], v197 offset:6656
	ds_read_b64_tr_b16 v[150:151], v199 offset:41984
	ds_read_b64_tr_b16 v[152:153], v199 offset:42496
	s_waitcnt lgkmcnt(11)
	v_mfma_f32_32x32x16_bf16 v[50:65], v[134:137], v[102:105], v[50:65]
	v_add_f32_e32 v83, v90, v91
	v_add_f32_e32 v84, v92, v93
	v_add_f32_e32 v83, v83, v84
	v_add_f32_e32 v82, v83, v82
	v_cvt_pk_bf16_f32 v142, v90, v91
	v_cvt_pk_bf16_f32 v143, v92, v93
	ds_read_b64_tr_b16 v[146:147], v199 offset:46080
	ds_read_b64_tr_b16 v[148:149], v199 offset:46592
	s_waitcnt lgkmcnt(12)
	v_mfma_f32_32x32x16_bf16 v[34:49], v[126:129], v[102:105], v[34:49]
	v_add_f32_e32 v83, v94, v95
	v_add_f32_e32 v84, v96, v97
	v_add_f32_e32 v83, v83, v84
	v_add_f32_e32 v82, v83, v82
	v_cvt_pk_bf16_f32 v144, v94, v95
	v_cvt_pk_bf16_f32 v145, v96, v97
	ds_read_b128 v[248:251], v197 offset:8192
	ds_read_b128 v[232:235], v197 offset:8704
	ds_read_b64_tr_b16 v[90:91], v199 offset:43008
	ds_read_b64_tr_b16 v[92:93], v199 offset:43520
	s_waitcnt lgkmcnt(14)
	v_mfma_f32_32x32x16_bf16 v[50:65], v[122:125], v[106:109], v[50:65]
	v_add_f32_e32 v83, v66, v67
	v_add_f32_e32 v84, v68, v69
	v_add_f32_e32 v83, v83, v84
	v_add_f32_e32 v84, v83, v82
	v_cvt_pk_bf16_f32 v82, v66, v67
	v_cvt_pk_bf16_f32 v83, v68, v69
	ds_read_b64_tr_b16 v[86:87], v199 offset:47104
	ds_read_b64_tr_b16 v[88:89], v199 offset:47616
	v_mfma_f32_32x32x16_bf16 v[34:49], v[118:121], v[106:109], v[34:49]
	v_add_f32_e32 v66, v70, v71
	v_add_f32_e32 v67, v72, v73
	v_add_f32_e32 v66, v66, v67
	v_add_f32_e32 v66, v66, v84
	v_cvt_pk_bf16_f32 v84, v70, v71
	v_cvt_pk_bf16_f32 v85, v72, v73
	ds_read_b64_tr_b16 v[70:71], v199 offset:44032
	ds_read_b64_tr_b16 v[72:73], v199 offset:44544
	s_waitcnt lgkmcnt(13)
	v_mfma_f32_32x32x16_bf16 v[50:65], v[170:173], v[110:113], v[50:65]
	v_add_f32_e32 v67, v74, v75
	v_add_f32_e32 v68, v76, v77
	v_add_f32_e32 v67, v67, v68
	v_add_f32_e32 v68, v67, v66
	v_cvt_pk_bf16_f32 v66, v74, v75
	v_cvt_pk_bf16_f32 v67, v76, v77
	ds_read_b64_tr_b16 v[74:75], v199 offset:48128
	ds_read_b64_tr_b16 v[76:77], v199 offset:48640
	s_waitcnt lgkmcnt(14)
	v_mfma_f32_32x32x16_bf16 v[34:49], v[174:177], v[110:113], v[34:49]
	v_add_f32_e32 v69, v78, v79
	v_add_f32_e32 v94, v80, v81
	v_add_f32_e32 v69, v69, v94
	v_add_f32_e32 v94, v69, v68
	v_cvt_pk_bf16_f32 v68, v78, v79
	v_cvt_pk_bf16_f32 v69, v80, v81
	s_waitcnt lgkmcnt(9)
	v_mfma_f32_32x32x16_bf16 v[50:65], v[248:251], v[114:117], v[50:65]
	s_waitcnt lgkmcnt(8)
	v_mfma_f32_32x32x16_bf16 v[34:49], v[232:235], v[114:117], v[34:49]
	s_add_i32 s54, s44, 3
	s_cmp_lt_i32 s54, s71
	s_cselect_b64 s[52:53], -1, 0
	s_cbranch_scc0 .LBB0_1334
	s_ashr_i32 s55, s54, 31
	s_and_b32 s45, s54, 3
	s_lshl_b64 s[58:59], s[54:55], 17
	s_mulk_i32 s45, 0x2800
	v_lshl_add_u64 v[78:79], v[212:213], 0, s[58:59]
	s_add_i32 s58, s45, s66
	s_mov_b32 m0, s58
	s_nop 0
	global_load_lds_dwordx4 v[78:79], off
	s_and_b64 vcc, exec, s[42:43]
	s_cbranch_vccnz .LBB0_1334
	s_lshl_b64 s[54:55], s[54:55], 11
	s_add_i32 s45, s45, s70
	v_lshl_add_u64 v[78:79], v[214:215], 0, s[54:55]
	s_mov_b32 m0, s45
	s_nop 0
	global_load_lds_dwordx4 v[78:79], off
.LBB0_1334:
	s_add_i32 s54, s44, 1
	s_cmp_lt_i32 s54, s71
	s_cselect_b64 s[58:59], -1, 0
	s_cbranch_scc0 .LBB0_1336
	s_mul_hi_i32 s45, s54, 0x55555556
	s_mul_i32 s45, s45, 3
	s_sub_i32 s45, s54, s45
	s_ashr_i32 s55, s54, 31
	s_lshl_b64 s[62:63], s[54:55], 17
	s_lshl_b32 s45, s45, 13
	v_lshl_add_u64 v[78:79], v[216:217], 0, s[62:63]
	s_add_i32 s45, s45, s72
	s_mov_b32 m0, s45
	s_nop 0
	global_load_lds_dwordx4 v[78:79], off

.LBB0_1368:
	s_setprio 0
	v_readlane_b32 s0, v255, 1
	v_readlane_b32 s10, v254, 0
	s_add_i32 s0, s0, 12
	v_readlane_b32 s11, v254, 1
	s_cmp_lt_i32 s0, s11
	s_cselect_b64 s[26:27], -1, 0
	s_and_b64 s[10:11], s[18:19], s[26:27]
	s_and_b64 vcc, exec, s[10:11]
	s_cbranch_vccz .LBB0_1414
	s_waitcnt vmcnt(0)
	s_waitcnt vmcnt(0) lgkmcnt(0)
	s_barrier
	s_mov_b64 s[18:19], exec
	v_readlane_b32 s10, v254, 46
	v_readlane_b32 s11, v254, 47
	s_and_b64 s[10:11], s[18:19], s[10:11]
	s_mov_b64 exec, s[10:11]
	s_cbranch_execz .LBB0_1413
	v_readlane_b32 s28, v254, 6
	v_readlane_b32 s1, v254, 8
	v_readlane_b32 s29, v254, 7
	s_waitcnt vmcnt(0) expcnt(0) lgkmcnt(0)
	v_mov_b32_e32 v2, s1
	ds_read_b32 v4, v2
	ds_read_b32 v2, v2 offset:4
	s_waitcnt lgkmcnt(1)
	v_cmp_ne_u32_e32 vcc, 0, v4
	s_cbranch_vccnz .LBB0_1384
	v_readlane_b32 s12, v254, 9
	s_add_u32 s30, s28, 0x1000
	v_readlane_b32 s13, v254, 10
	s_addc_u32 s31, s29, 0
	s_load_dwordx2 s[10:11], s[12:13], 0x0
	s_load_dword s1, s[12:13], 0x8
	s_add_u32 s34, s28, 0x1100
	s_addc_u32 s35, s29, 0
	s_add_u32 s36, s28, 0x1200
	s_addc_u32 s37, s29, 0
	s_waitcnt lgkmcnt(0)
	s_mul_i32 s8, s11, s10
	s_add_u32 s38, s28, 0x1300
	s_mul_i32 s1, s8, s1
	s_addc_u32 s39, s29, 0
	s_mov_b32 s8, 1
	s_mov_b64 s[40:41], 0
	s_branch .LBB0_1374
